# grid barrier arrival: arrive atomic issued before buffer_inv sc1 and waited alone with vmcnt(1); the invalidate completes under the later vmcnt(0) of each path
# baseline (speedup 1.0000x reference)
.LBB0_190:
	s_or_b64 exec, exec, s[6:7]
	v_cvt_f32_u32_e32 v4, v2
	s_waitcnt vmcnt(1)
	v_readfirstlane_b32 s4, v3
	v_sub_u32_e32 v3, 0, v2
	v_rcp_iflag_f32_e32 v4, v4
	v_add_u32_e32 v5, s4, v1
	v_mul_f32_e32 v4, 0x4f7ffffe, v4
	v_cvt_u32_f32_e32 v4, v4
	v_mul_lo_u32 v1, v3, v4
	v_mul_hi_u32 v1, v4, v1
	v_add_u32_e32 v1, v4, v1
	v_mul_hi_u32 v1, v5, v1
	v_mul_lo_u32 v3, v1, v2
	v_sub_u32_e32 v3, v5, v3
	v_add_u32_e32 v4, 1, v1
	v_cmp_ge_u32_e32 vcc, v3, v2
	s_nop 1
	v_cndmask_b32_e32 v1, v1, v4, vcc
	v_sub_u32_e32 v4, v3, v2
	v_cndmask_b32_e32 v3, v3, v4, vcc
	v_add_u32_e32 v4, 1, v1
	v_cmp_ge_u32_e32 vcc, v3, v2
	v_add_u32_e32 v3, 1, v5
	s_nop 0
	v_cndmask_b32_e32 v1, v1, v4, vcc
	v_mul_lo_u32 v4, v2, v1
	v_add_u32_e32 v2, v4, v2
	v_readfirstlane_b32 s99, v1
	v_cmp_ne_u32_e32 vcc, v3, v2
	s_and_saveexec_b64 s[4:5], vcc
	s_xor_b64 s[4:5], exec, s[4:5]
	s_cbranch_execz .LBB0_204
	s_waitcnt lgkmcnt(0)
	v_mov_b32_e32 v0, 0x2000
	global_load_dword v0, v0, s[2:3] offset:1024 sc1
	s_add_u32 s8, s2, 0x2400
	s_addc_u32 s9, s3, 0
	s_waitcnt vmcnt(0)
	v_cmp_eq_u32_e32 vcc, v0, v1
	s_and_saveexec_b64 s[6:7], vcc
	s_cbranch_execz .LBB0_203
	s_mov_b32 s16, 1
	s_mov_b64 s[10:11], 0
	v_mov_b32_e32 v0, 0
	s_branch .LBB0_194

.LBB0_266:
	s_or_b64 exec, exec, s[8:9]
	v_cvt_f32_u32_e32 v4, v2
	s_waitcnt vmcnt(1)
	v_readfirstlane_b32 s6, v3
	v_sub_u32_e32 v3, 0, v2
	v_rcp_iflag_f32_e32 v4, v4
	v_add_u32_e32 v5, s6, v1
	v_mul_f32_e32 v4, 0x4f7ffffe, v4
	v_cvt_u32_f32_e32 v4, v4
	v_mul_lo_u32 v1, v3, v4
	v_mul_hi_u32 v1, v4, v1
	v_add_u32_e32 v1, v4, v1
	v_mul_hi_u32 v1, v5, v1
	v_mul_lo_u32 v3, v1, v2
	v_sub_u32_e32 v3, v5, v3
	v_add_u32_e32 v4, 1, v1
	v_cmp_ge_u32_e32 vcc, v3, v2
	s_nop 1
	v_cndmask_b32_e32 v1, v1, v4, vcc
	v_sub_u32_e32 v4, v3, v2
	v_cndmask_b32_e32 v3, v3, v4, vcc
	v_add_u32_e32 v4, 1, v1
	v_cmp_ge_u32_e32 vcc, v3, v2
	v_add_u32_e32 v3, 1, v5
	s_nop 0
	v_cndmask_b32_e32 v1, v1, v4, vcc
	v_mul_lo_u32 v4, v2, v1
	v_add_u32_e32 v2, v4, v2
	v_readfirstlane_b32 s99, v1
	v_cmp_ne_u32_e32 vcc, v3, v2
	s_and_saveexec_b64 s[6:7], vcc
	s_xor_b64 s[6:7], exec, s[6:7]
	s_cbranch_execz .LBB0_280
	s_waitcnt lgkmcnt(0)
	v_mov_b32_e32 v0, 0x2000
	global_load_dword v0, v0, s[2:3] offset:1024 sc1
	s_add_u32 s10, s2, 0x2400
	s_addc_u32 s11, s3, 0
	s_waitcnt vmcnt(0)
	v_cmp_eq_u32_e32 vcc, v0, v1
	s_and_saveexec_b64 s[8:9], vcc
	s_cbranch_execz .LBB0_279
	s_mov_b32 s16, 1
	s_mov_b64 s[12:13], 0
	v_mov_b32_e32 v0, 0
	s_branch .LBB0_270

.LBB0_690:
	s_or_b64 exec, exec, s[6:7]
	v_cvt_f32_u32_e32 v4, v2
	s_waitcnt vmcnt(1)
	v_readfirstlane_b32 s4, v3
	v_sub_u32_e32 v3, 0, v2
	v_rcp_iflag_f32_e32 v4, v4
	v_add_u32_e32 v5, s4, v1
	v_mul_f32_e32 v4, 0x4f7ffffe, v4
	v_cvt_u32_f32_e32 v4, v4
	v_mul_lo_u32 v1, v3, v4
	v_mul_hi_u32 v1, v4, v1
	v_add_u32_e32 v1, v4, v1
	v_mul_hi_u32 v1, v5, v1
	v_mul_lo_u32 v3, v1, v2
	v_sub_u32_e32 v3, v5, v3
	v_add_u32_e32 v4, 1, v1
	v_cmp_ge_u32_e32 vcc, v3, v2
	s_nop 1
	v_cndmask_b32_e32 v1, v1, v4, vcc
	v_sub_u32_e32 v4, v3, v2
	v_cndmask_b32_e32 v3, v3, v4, vcc
	v_add_u32_e32 v4, 1, v1
	v_cmp_ge_u32_e32 vcc, v3, v2
	v_add_u32_e32 v3, 1, v5
	s_nop 0
	v_cndmask_b32_e32 v1, v1, v4, vcc
	v_mul_lo_u32 v4, v2, v1
	v_add_u32_e32 v2, v4, v2
	v_readfirstlane_b32 s99, v1
	v_cmp_ne_u32_e32 vcc, v3, v2
	s_and_saveexec_b64 s[4:5], vcc
	s_xor_b64 s[4:5], exec, s[4:5]
	s_cbranch_execz .LBB0_704
	s_waitcnt lgkmcnt(0)
	v_mov_b32_e32 v0, 0x2000
	global_load_dword v0, v0, s[2:3] offset:1024 sc1
	s_add_u32 s10, s2, 0x2400
	s_addc_u32 s11, s3, 0
	s_waitcnt vmcnt(0)
	v_cmp_eq_u32_e32 vcc, v0, v1
	s_and_saveexec_b64 s[6:7], vcc
	s_cbranch_execz .LBB0_703
	s_mov_b32 s18, 1
	s_mov_b64 s[12:13], 0
	v_mov_b32_e32 v0, 0
	s_branch .LBB0_694

.LBB0_760:
	s_or_b64 exec, exec, s[6:7]
	v_cvt_f32_u32_e32 v4, v2
	s_waitcnt vmcnt(1)
	v_readfirstlane_b32 s4, v3
	v_sub_u32_e32 v3, 0, v2
	v_rcp_iflag_f32_e32 v4, v4
	v_add_u32_e32 v5, s4, v1
	v_mul_f32_e32 v4, 0x4f7ffffe, v4
	v_cvt_u32_f32_e32 v4, v4
	v_mul_lo_u32 v1, v3, v4
	v_mul_hi_u32 v1, v4, v1
	v_add_u32_e32 v1, v4, v1
	v_mul_hi_u32 v1, v5, v1
	v_mul_lo_u32 v3, v1, v2
	v_sub_u32_e32 v3, v5, v3
	v_add_u32_e32 v4, 1, v1
	v_cmp_ge_u32_e32 vcc, v3, v2
	s_nop 1
	v_cndmask_b32_e32 v1, v1, v4, vcc
	v_sub_u32_e32 v4, v3, v2
	v_cndmask_b32_e32 v3, v3, v4, vcc
	v_add_u32_e32 v4, 1, v1
	v_cmp_ge_u32_e32 vcc, v3, v2
	v_add_u32_e32 v3, 1, v5
	s_nop 0
	v_cndmask_b32_e32 v1, v1, v4, vcc
	v_mul_lo_u32 v4, v2, v1
	v_add_u32_e32 v2, v4, v2
	v_readfirstlane_b32 s99, v1
	v_cmp_ne_u32_e32 vcc, v3, v2
	s_and_saveexec_b64 s[4:5], vcc
	s_xor_b64 s[4:5], exec, s[4:5]
	s_cbranch_execz .LBB0_774
	s_waitcnt lgkmcnt(0)
	v_mov_b32_e32 v0, 0x2000
	global_load_dword v0, v0, s[2:3] offset:1024 sc1
	s_add_u32 s12, s2, 0x2400
	s_addc_u32 s13, s3, 0
	s_waitcnt vmcnt(0)
	v_cmp_eq_u32_e32 vcc, v0, v1
	s_and_saveexec_b64 s[6:7], vcc
	s_cbranch_execz .LBB0_773
	s_mov_b32 s18, 1
	s_mov_b64 s[14:15], 0
	v_mov_b32_e32 v0, 0
	s_branch .LBB0_764

.LBB0_858:
	s_or_b64 exec, exec, s[12:13]
	v_cvt_f32_u32_e32 v4, v2
	s_waitcnt vmcnt(1)
	v_readfirstlane_b32 s4, v3
	v_sub_u32_e32 v3, 0, v2
	v_rcp_iflag_f32_e32 v4, v4
	v_add_u32_e32 v5, s4, v1
	v_mul_f32_e32 v4, 0x4f7ffffe, v4
	v_cvt_u32_f32_e32 v4, v4
	v_mul_lo_u32 v1, v3, v4
	v_mul_hi_u32 v1, v4, v1
	v_add_u32_e32 v1, v4, v1
	v_mul_hi_u32 v1, v5, v1
	v_mul_lo_u32 v3, v1, v2
	v_sub_u32_e32 v3, v5, v3
	v_add_u32_e32 v4, 1, v1
	v_cmp_ge_u32_e32 vcc, v3, v2
	s_nop 1
	v_cndmask_b32_e32 v1, v1, v4, vcc
	v_sub_u32_e32 v4, v3, v2
	v_cndmask_b32_e32 v3, v3, v4, vcc
	v_add_u32_e32 v4, 1, v1
	v_cmp_ge_u32_e32 vcc, v3, v2
	v_add_u32_e32 v3, 1, v5
	s_nop 0
	v_cndmask_b32_e32 v1, v1, v4, vcc
	v_mul_lo_u32 v4, v2, v1
	v_add_u32_e32 v2, v4, v2
	v_readfirstlane_b32 s99, v1
	v_cmp_ne_u32_e32 vcc, v3, v2
	s_and_saveexec_b64 s[4:5], vcc
	s_xor_b64 s[4:5], exec, s[4:5]
	s_cbranch_execz .LBB0_872
	s_waitcnt lgkmcnt(0)
	v_mov_b32_e32 v0, 0x2000
	global_load_dword v0, v0, s[2:3] offset:1024 sc1
	s_add_u32 s14, s2, 0x2400
	s_addc_u32 s15, s3, 0
	s_waitcnt vmcnt(0)
	v_cmp_eq_u32_e32 vcc, v0, v1
	s_and_saveexec_b64 s[12:13], vcc
	s_cbranch_execz .LBB0_871
	s_mov_b32 s18, 1
	s_mov_b64 s[16:17], 0
	v_mov_b32_e32 v0, 0
	s_branch .LBB0_862

.LBB0_948:
	s_or_b64 exec, exec, s[12:13]
	v_cvt_f32_u32_e32 v4, v2
	s_waitcnt vmcnt(1)
	v_readfirstlane_b32 s6, v3
	v_sub_u32_e32 v3, 0, v2
	v_rcp_iflag_f32_e32 v4, v4
	v_add_u32_e32 v5, s6, v1
	v_mul_f32_e32 v4, 0x4f7ffffe, v4
	v_cvt_u32_f32_e32 v4, v4
	v_mul_lo_u32 v1, v3, v4
	v_mul_hi_u32 v1, v4, v1
	v_add_u32_e32 v1, v4, v1
	v_mul_hi_u32 v1, v5, v1
	v_mul_lo_u32 v3, v1, v2
	v_sub_u32_e32 v3, v5, v3
	v_add_u32_e32 v4, 1, v1
	v_cmp_ge_u32_e32 vcc, v3, v2
	s_nop 1
	v_cndmask_b32_e32 v1, v1, v4, vcc
	v_sub_u32_e32 v4, v3, v2
	v_cndmask_b32_e32 v3, v3, v4, vcc
	v_add_u32_e32 v4, 1, v1
	v_cmp_ge_u32_e32 vcc, v3, v2
	v_add_u32_e32 v3, 1, v5
	s_nop 0
	v_cndmask_b32_e32 v1, v1, v4, vcc
	v_mul_lo_u32 v4, v2, v1
	v_add_u32_e32 v2, v4, v2
	v_readfirstlane_b32 s99, v1
	v_cmp_ne_u32_e32 vcc, v3, v2
	s_and_saveexec_b64 s[6:7], vcc
	s_xor_b64 s[6:7], exec, s[6:7]
	s_cbranch_execz .LBB0_962
	s_waitcnt lgkmcnt(0)
	v_mov_b32_e32 v0, 0x2000
	global_load_dword v0, v0, s[4:5] offset:1024 sc1
	s_add_u32 s14, s4, 0x2400
	s_addc_u32 s15, s5, 0
	s_waitcnt vmcnt(0)
	v_cmp_eq_u32_e32 vcc, v0, v1
	s_and_saveexec_b64 s[12:13], vcc
	s_cbranch_execz .LBB0_961
	s_mov_b32 s18, 1
	s_mov_b64 s[16:17], 0
	v_mov_b32_e32 v0, 0
	s_branch .LBB0_952

.LBB0_1128:
	s_or_b64 exec, exec, s[6:7]
	v_cvt_f32_u32_e32 v4, v2
	s_waitcnt vmcnt(1)
	v_readfirstlane_b32 s4, v3
	v_sub_u32_e32 v3, 0, v2
	v_rcp_iflag_f32_e32 v4, v4
	v_add_u32_e32 v5, s4, v1
	v_mul_f32_e32 v4, 0x4f7ffffe, v4
	v_cvt_u32_f32_e32 v4, v4
	v_mul_lo_u32 v1, v3, v4
	v_mul_hi_u32 v1, v4, v1
	v_add_u32_e32 v1, v4, v1
	v_mul_hi_u32 v1, v5, v1
	v_mul_lo_u32 v3, v1, v2
	v_sub_u32_e32 v3, v5, v3
	v_add_u32_e32 v4, 1, v1
	v_cmp_ge_u32_e32 vcc, v3, v2
	s_nop 1
	v_cndmask_b32_e32 v1, v1, v4, vcc
	v_sub_u32_e32 v4, v3, v2
	v_cndmask_b32_e32 v3, v3, v4, vcc
	v_add_u32_e32 v4, 1, v1
	v_cmp_ge_u32_e32 vcc, v3, v2
	v_add_u32_e32 v3, 1, v5
	s_nop 0
	v_cndmask_b32_e32 v1, v1, v4, vcc
	v_mul_lo_u32 v4, v2, v1
	v_add_u32_e32 v2, v4, v2
	v_readfirstlane_b32 s99, v1
	v_cmp_ne_u32_e32 vcc, v3, v2
	s_and_saveexec_b64 s[4:5], vcc
	s_xor_b64 s[4:5], exec, s[4:5]
	s_cbranch_execz .LBB0_1142
	s_waitcnt lgkmcnt(0)
	v_mov_b32_e32 v0, 0x2000
	global_load_dword v0, v0, s[2:3] offset:1024 sc1
	s_add_u32 s8, s2, 0x2400
	s_addc_u32 s9, s3, 0
	s_waitcnt vmcnt(0)
	v_cmp_eq_u32_e32 vcc, v0, v1
	s_and_saveexec_b64 s[6:7], vcc
	s_cbranch_execz .LBB0_1141
	s_mov_b32 s18, 1
	s_mov_b64 s[10:11], 0
	v_mov_b32_e32 v0, 0
	s_branch .LBB0_1132

.LBB0_1735:
	s_or_b64 exec, exec, s[8:9]
	v_cvt_f32_u32_e32 v4, v2
	s_waitcnt vmcnt(1)
	v_readfirstlane_b32 s4, v3
	v_sub_u32_e32 v3, 0, v2
	v_rcp_iflag_f32_e32 v4, v4
	v_add_u32_e32 v5, s4, v1
	v_mul_f32_e32 v4, 0x4f7ffffe, v4
	v_cvt_u32_f32_e32 v4, v4
	v_mul_lo_u32 v1, v3, v4
	v_mul_hi_u32 v1, v4, v1
	v_add_u32_e32 v1, v4, v1
	v_mul_hi_u32 v1, v5, v1
	v_mul_lo_u32 v3, v1, v2
	v_sub_u32_e32 v3, v5, v3
	v_add_u32_e32 v4, 1, v1
	v_cmp_ge_u32_e32 vcc, v3, v2
	s_nop 1
	v_cndmask_b32_e32 v1, v1, v4, vcc
	v_sub_u32_e32 v4, v3, v2
	v_cndmask_b32_e32 v3, v3, v4, vcc
	v_add_u32_e32 v4, 1, v1
	v_cmp_ge_u32_e32 vcc, v3, v2
	v_add_u32_e32 v3, 1, v5
	s_nop 0
	v_cndmask_b32_e32 v1, v1, v4, vcc
	v_mul_lo_u32 v4, v2, v1
	v_add_u32_e32 v2, v4, v2
	v_readfirstlane_b32 s99, v1
	v_cmp_ne_u32_e32 vcc, v3, v2
	s_and_saveexec_b64 s[4:5], vcc
	s_xor_b64 s[4:5], exec, s[4:5]
	s_cbranch_execz .LBB0_1749
	s_waitcnt lgkmcnt(0)
	v_mov_b32_e32 v0, 0x2000
	global_load_dword v0, v0, s[2:3] offset:1024 sc1
	s_add_u32 s10, s2, 0x2400
	s_addc_u32 s11, s3, 0
	s_waitcnt vmcnt(0)
	v_cmp_eq_u32_e32 vcc, v0, v1
	s_and_saveexec_b64 s[8:9], vcc
	s_cbranch_execz .LBB0_1748
	s_mov_b32 s18, 1
	s_mov_b64 s[12:13], 0
	v_mov_b32_e32 v0, 0
	s_branch .LBB0_1739

.LBB0_1825:
	s_or_b64 exec, exec, s[8:9]
	v_cvt_f32_u32_e32 v4, v2
	s_waitcnt vmcnt(1)
	v_readfirstlane_b32 s6, v3
	v_sub_u32_e32 v3, 0, v2
	v_rcp_iflag_f32_e32 v4, v4
	v_add_u32_e32 v5, s6, v1
	v_mul_f32_e32 v4, 0x4f7ffffe, v4
	v_cvt_u32_f32_e32 v4, v4
	v_mul_lo_u32 v1, v3, v4
	v_mul_hi_u32 v1, v4, v1
	v_add_u32_e32 v1, v4, v1
	v_mul_hi_u32 v1, v5, v1
	v_mul_lo_u32 v3, v1, v2
	v_sub_u32_e32 v3, v5, v3
	v_add_u32_e32 v4, 1, v1
	v_cmp_ge_u32_e32 vcc, v3, v2
	s_nop 1
	v_cndmask_b32_e32 v1, v1, v4, vcc
	v_sub_u32_e32 v4, v3, v2
	v_cndmask_b32_e32 v3, v3, v4, vcc
	v_add_u32_e32 v4, 1, v1
	v_cmp_ge_u32_e32 vcc, v3, v2
	v_add_u32_e32 v3, 1, v5
	s_nop 0
	v_cndmask_b32_e32 v1, v1, v4, vcc
	v_mul_lo_u32 v4, v2, v1
	v_add_u32_e32 v2, v4, v2
	v_readfirstlane_b32 s99, v1
	v_cmp_ne_u32_e32 vcc, v3, v2
	s_and_saveexec_b64 s[6:7], vcc
	s_xor_b64 s[6:7], exec, s[6:7]
	s_cbranch_execz .LBB0_1839
	s_waitcnt lgkmcnt(0)
	v_mov_b32_e32 v0, 0x2000
	global_load_dword v0, v0, s[4:5] offset:1024 sc1
	s_add_u32 s10, s4, 0x2400
	s_addc_u32 s11, s5, 0
	s_waitcnt vmcnt(0)
	v_cmp_eq_u32_e32 vcc, v0, v1
	s_and_saveexec_b64 s[8:9], vcc
	s_cbranch_execz .LBB0_1838
	s_mov_b32 s18, 1
	s_mov_b64 s[12:13], 0
	v_mov_b32_e32 v0, 0
	s_branch .LBB0_1829

.LBB0_2327:
	s_or_b64 exec, exec, s[6:7]
	v_cvt_f32_u32_e32 v4, v2
	s_waitcnt vmcnt(1)
	v_readfirstlane_b32 s4, v3
	v_sub_u32_e32 v3, 0, v2
	v_rcp_iflag_f32_e32 v4, v4
	v_add_u32_e32 v5, s4, v1
	v_mul_f32_e32 v4, 0x4f7ffffe, v4
	v_cvt_u32_f32_e32 v4, v4
	v_mul_lo_u32 v1, v3, v4
	v_mul_hi_u32 v1, v4, v1
	v_add_u32_e32 v1, v4, v1
	v_mul_hi_u32 v1, v5, v1
	v_mul_lo_u32 v3, v1, v2
	v_sub_u32_e32 v3, v5, v3
	v_add_u32_e32 v4, 1, v1
	v_cmp_ge_u32_e32 vcc, v3, v2
	s_nop 1
	v_cndmask_b32_e32 v1, v1, v4, vcc
	v_sub_u32_e32 v4, v3, v2
	v_cndmask_b32_e32 v3, v3, v4, vcc
	v_add_u32_e32 v4, 1, v1
	v_cmp_ge_u32_e32 vcc, v3, v2
	v_add_u32_e32 v3, 1, v5
	s_nop 0
	v_cndmask_b32_e32 v1, v1, v4, vcc
	v_mul_lo_u32 v4, v2, v1
	v_add_u32_e32 v2, v4, v2
	v_readfirstlane_b32 s99, v1
	v_cmp_ne_u32_e32 vcc, v3, v2
	s_and_saveexec_b64 s[4:5], vcc
	s_xor_b64 s[4:5], exec, s[4:5]
	s_cbranch_execz .LBB0_2341
	s_waitcnt lgkmcnt(0)
	v_mov_b32_e32 v0, 0x2000
	global_load_dword v0, v0, s[2:3] offset:1024 sc1
	s_add_u32 s8, s2, 0x2400
	s_addc_u32 s9, s3, 0
	s_waitcnt vmcnt(0)
	v_cmp_eq_u32_e32 vcc, v0, v1
	s_and_saveexec_b64 s[6:7], vcc
	s_cbranch_execz .LBB0_2340
	s_mov_b32 s20, 1
	s_mov_b64 s[10:11], 0
	v_mov_b32_e32 v0, 0
	s_branch .LBB0_2331

.LBB0_2446:
	s_or_b64 exec, exec, s[6:7]
	v_cvt_f32_u32_e32 v4, v2
	s_waitcnt vmcnt(1)
	v_readfirstlane_b32 s4, v3
	v_sub_u32_e32 v3, 0, v2
	v_rcp_iflag_f32_e32 v4, v4
	v_add_u32_e32 v5, s4, v1
	v_mul_f32_e32 v4, 0x4f7ffffe, v4
	v_cvt_u32_f32_e32 v4, v4
	v_mul_lo_u32 v1, v3, v4
	v_mul_hi_u32 v1, v4, v1
	v_add_u32_e32 v1, v4, v1
	v_mul_hi_u32 v1, v5, v1
	v_mul_lo_u32 v3, v1, v2
	v_sub_u32_e32 v3, v5, v3
	v_add_u32_e32 v4, 1, v1
	v_cmp_ge_u32_e32 vcc, v3, v2
	s_nop 1
	v_cndmask_b32_e32 v1, v1, v4, vcc
	v_sub_u32_e32 v4, v3, v2
	v_cndmask_b32_e32 v3, v3, v4, vcc
	v_add_u32_e32 v4, 1, v1
	v_cmp_ge_u32_e32 vcc, v3, v2
	v_add_u32_e32 v3, 1, v5
	s_nop 0
	v_cndmask_b32_e32 v1, v1, v4, vcc
	v_mul_lo_u32 v4, v2, v1
	v_add_u32_e32 v2, v4, v2
	v_readfirstlane_b32 s99, v1
	v_cmp_ne_u32_e32 vcc, v3, v2
	s_and_saveexec_b64 s[4:5], vcc
	s_xor_b64 s[4:5], exec, s[4:5]
	s_cbranch_execz .LBB0_2460
	s_waitcnt lgkmcnt(0)
	v_mov_b32_e32 v0, 0x2000
	global_load_dword v0, v0, s[2:3] offset:1024 sc1
	s_add_u32 s8, s2, 0x2400
	s_addc_u32 s9, s3, 0
	s_waitcnt vmcnt(0)
	v_cmp_eq_u32_e32 vcc, v0, v1
	s_and_saveexec_b64 s[6:7], vcc
	s_cbranch_execz .LBB0_2459
	s_mov_b32 s24, 1
	s_mov_b64 s[10:11], 0
	v_mov_b32_e32 v0, 0
	s_branch .LBB0_2450

.LBB0_2516:
	s_or_b64 exec, exec, s[6:7]
	v_cvt_f32_u32_e32 v4, v2
	s_waitcnt vmcnt(1)
	v_readfirstlane_b32 s4, v3
	v_sub_u32_e32 v3, 0, v2
	v_rcp_iflag_f32_e32 v4, v4
	v_add_u32_e32 v5, s4, v1
	v_mul_f32_e32 v4, 0x4f7ffffe, v4
	v_cvt_u32_f32_e32 v4, v4
	v_mul_lo_u32 v1, v3, v4
	v_mul_hi_u32 v1, v4, v1
	v_add_u32_e32 v1, v4, v1
	v_mul_hi_u32 v1, v5, v1
	v_mul_lo_u32 v3, v1, v2
	v_sub_u32_e32 v3, v5, v3
	v_add_u32_e32 v4, 1, v1
	v_cmp_ge_u32_e32 vcc, v3, v2
	s_nop 1
	v_cndmask_b32_e32 v1, v1, v4, vcc
	v_sub_u32_e32 v4, v3, v2
	v_cndmask_b32_e32 v3, v3, v4, vcc
	v_add_u32_e32 v4, 1, v1
	v_cmp_ge_u32_e32 vcc, v3, v2
	v_add_u32_e32 v3, 1, v5
	s_nop 0
	v_cndmask_b32_e32 v1, v1, v4, vcc
	v_mul_lo_u32 v4, v2, v1
	v_add_u32_e32 v2, v4, v2
	v_readfirstlane_b32 s99, v1
	v_cmp_ne_u32_e32 vcc, v3, v2
	s_and_saveexec_b64 s[4:5], vcc
	s_xor_b64 s[4:5], exec, s[4:5]
	s_cbranch_execz .LBB0_2530
	s_waitcnt lgkmcnt(0)
	v_mov_b32_e32 v0, 0x2000
	global_load_dword v0, v0, s[2:3] offset:1024 sc1
	s_add_u32 s8, s2, 0x2400
	s_addc_u32 s9, s3, 0
	s_waitcnt vmcnt(0)
	v_cmp_eq_u32_e32 vcc, v0, v1
	s_and_saveexec_b64 s[6:7], vcc
	s_cbranch_execz .LBB0_2529
	s_mov_b32 s26, 1
	s_mov_b64 s[10:11], 0
	v_mov_b32_e32 v0, 0
	s_branch .LBB0_2520

.LBB0_2614:
	s_or_b64 exec, exec, s[8:9]
	v_cvt_f32_u32_e32 v4, v2
	s_waitcnt vmcnt(1)
	v_readfirstlane_b32 s4, v3
	v_sub_u32_e32 v3, 0, v2
	v_rcp_iflag_f32_e32 v4, v4
	v_add_u32_e32 v5, s4, v1
	v_mul_f32_e32 v4, 0x4f7ffffe, v4
	v_cvt_u32_f32_e32 v4, v4
	v_mul_lo_u32 v1, v3, v4
	v_mul_hi_u32 v1, v4, v1
	v_add_u32_e32 v1, v4, v1
	v_mul_hi_u32 v1, v5, v1
	v_mul_lo_u32 v3, v1, v2
	v_sub_u32_e32 v3, v5, v3
	v_add_u32_e32 v4, 1, v1
	v_cmp_ge_u32_e32 vcc, v3, v2
	s_nop 1
	v_cndmask_b32_e32 v1, v1, v4, vcc
	v_sub_u32_e32 v4, v3, v2
	v_cndmask_b32_e32 v3, v3, v4, vcc
	v_add_u32_e32 v4, 1, v1
	v_cmp_ge_u32_e32 vcc, v3, v2
	v_add_u32_e32 v3, 1, v5
	s_nop 0
	v_cndmask_b32_e32 v1, v1, v4, vcc
	v_mul_lo_u32 v4, v2, v1
	v_add_u32_e32 v2, v4, v2
	v_readfirstlane_b32 s99, v1
	v_cmp_ne_u32_e32 vcc, v3, v2
	s_and_saveexec_b64 s[4:5], vcc
	s_xor_b64 s[4:5], exec, s[4:5]
	s_cbranch_execz .LBB0_2628
	s_waitcnt lgkmcnt(0)
	v_mov_b32_e32 v0, 0x2000
	global_load_dword v0, v0, s[2:3] offset:1024 sc1
	s_add_u32 s10, s2, 0x2400
	s_addc_u32 s11, s3, 0
	s_waitcnt vmcnt(0)
	v_cmp_eq_u32_e32 vcc, v0, v1
	s_and_saveexec_b64 s[8:9], vcc
	s_cbranch_execz .LBB0_2627
	s_mov_b32 s28, 1
	s_mov_b64 s[12:13], 0
	v_mov_b32_e32 v0, 0
	s_branch .LBB0_2618

.LBB0_2704:
	s_or_b64 exec, exec, s[8:9]
	v_cvt_f32_u32_e32 v4, v2
	s_waitcnt vmcnt(1)
	v_readfirstlane_b32 s6, v3
	v_sub_u32_e32 v3, 0, v2
	v_rcp_iflag_f32_e32 v4, v4
	v_add_u32_e32 v5, s6, v1
	v_mul_f32_e32 v4, 0x4f7ffffe, v4
	v_cvt_u32_f32_e32 v4, v4
	v_mul_lo_u32 v1, v3, v4
	v_mul_hi_u32 v1, v4, v1
	v_add_u32_e32 v1, v4, v1
	v_mul_hi_u32 v1, v5, v1
	v_mul_lo_u32 v3, v1, v2
	v_sub_u32_e32 v3, v5, v3
	v_add_u32_e32 v4, 1, v1
	v_cmp_ge_u32_e32 vcc, v3, v2
	s_nop 1
	v_cndmask_b32_e32 v1, v1, v4, vcc
	v_sub_u32_e32 v4, v3, v2
	v_cndmask_b32_e32 v3, v3, v4, vcc
	v_add_u32_e32 v4, 1, v1
	v_cmp_ge_u32_e32 vcc, v3, v2
	v_add_u32_e32 v3, 1, v5
	s_nop 0
	v_cndmask_b32_e32 v1, v1, v4, vcc
	v_mul_lo_u32 v4, v2, v1
	v_add_u32_e32 v2, v4, v2
	v_readfirstlane_b32 s99, v1
	v_cmp_ne_u32_e32 vcc, v3, v2
	s_and_saveexec_b64 s[6:7], vcc
	s_xor_b64 s[6:7], exec, s[6:7]
	s_cbranch_execz .LBB0_2718
	s_waitcnt lgkmcnt(0)
	v_mov_b32_e32 v0, 0x2000
	global_load_dword v0, v0, s[4:5] offset:1024 sc1
	s_add_u32 s10, s4, 0x2400
	s_addc_u32 s11, s5, 0
	s_waitcnt vmcnt(0)
	v_cmp_eq_u32_e32 vcc, v0, v1
	s_and_saveexec_b64 s[8:9], vcc
	s_cbranch_execz .LBB0_2717
	s_mov_b32 s28, 1
	s_mov_b64 s[12:13], 0
	v_mov_b32_e32 v0, 0
	s_branch .LBB0_2708

.LBB0_2962:
	s_or_b64 exec, exec, s[8:9]
	v_cvt_f32_u32_e32 v4, v2
	s_waitcnt vmcnt(1)
	v_readfirstlane_b32 s6, v3
	v_sub_u32_e32 v3, 0, v2
	v_rcp_iflag_f32_e32 v4, v4
	v_add_u32_e32 v5, s6, v1
	v_mul_f32_e32 v4, 0x4f7ffffe, v4
	v_cvt_u32_f32_e32 v4, v4
	v_mul_lo_u32 v1, v3, v4
	v_mul_hi_u32 v1, v4, v1
	v_add_u32_e32 v1, v4, v1
	v_mul_hi_u32 v1, v5, v1
	v_mul_lo_u32 v3, v1, v2
	v_sub_u32_e32 v3, v5, v3
	v_add_u32_e32 v4, 1, v1
	v_cmp_ge_u32_e32 vcc, v3, v2
	s_nop 1
	v_cndmask_b32_e32 v1, v1, v4, vcc
	v_sub_u32_e32 v4, v3, v2
	v_cndmask_b32_e32 v3, v3, v4, vcc
	v_add_u32_e32 v4, 1, v1
	v_cmp_ge_u32_e32 vcc, v3, v2
	v_add_u32_e32 v3, 1, v5
	s_nop 0
	v_cndmask_b32_e32 v1, v1, v4, vcc
	v_mul_lo_u32 v4, v2, v1
	v_add_u32_e32 v2, v4, v2
	v_readfirstlane_b32 s99, v1
	v_cmp_ne_u32_e32 vcc, v3, v2
	s_and_saveexec_b64 s[6:7], vcc
	s_xor_b64 s[6:7], exec, s[6:7]
	s_cbranch_execz .LBB0_2976
	s_waitcnt lgkmcnt(0)
	v_mov_b32_e32 v0, 0x2000
	global_load_dword v0, v0, s[4:5] offset:1024 sc1
	s_add_u32 s10, s4, 0x2400
	s_addc_u32 s11, s5, 0
	s_waitcnt vmcnt(0)
	v_cmp_eq_u32_e32 vcc, v0, v1
	s_and_saveexec_b64 s[8:9], vcc
	s_cbranch_execz .LBB0_2975
	s_mov_b32 s22, 1
	s_mov_b64 s[12:13], 0
	v_mov_b32_e32 v0, 0
	s_branch .LBB0_2966

.LBB0_3194:
	s_or_b64 exec, exec, s[6:7]
	v_cvt_f32_u32_e32 v4, v2
	s_waitcnt vmcnt(1)
	v_readfirstlane_b32 s4, v3
	v_sub_u32_e32 v3, 0, v2
	v_rcp_iflag_f32_e32 v4, v4
	v_add_u32_e32 v5, s4, v1
	v_mul_f32_e32 v4, 0x4f7ffffe, v4
	v_cvt_u32_f32_e32 v4, v4
	v_mul_lo_u32 v1, v3, v4
	v_mul_hi_u32 v1, v4, v1
	v_add_u32_e32 v1, v4, v1
	v_mul_hi_u32 v1, v5, v1
	v_mul_lo_u32 v3, v1, v2
	v_sub_u32_e32 v3, v5, v3
	v_add_u32_e32 v4, 1, v1
	v_cmp_ge_u32_e32 vcc, v3, v2
	s_nop 1
	v_cndmask_b32_e32 v1, v1, v4, vcc
	v_sub_u32_e32 v4, v3, v2
	v_cndmask_b32_e32 v3, v3, v4, vcc
	v_add_u32_e32 v4, 1, v1
	v_cmp_ge_u32_e32 vcc, v3, v2
	v_add_u32_e32 v3, 1, v5
	s_nop 0
	v_cndmask_b32_e32 v1, v1, v4, vcc
	v_mul_lo_u32 v4, v2, v1
	v_add_u32_e32 v2, v4, v2
	v_readfirstlane_b32 s99, v1
	v_cmp_ne_u32_e32 vcc, v3, v2
	s_and_saveexec_b64 s[4:5], vcc
	s_xor_b64 s[4:5], exec, s[4:5]
	s_cbranch_execz .LBB0_3208
	s_waitcnt lgkmcnt(0)
	v_mov_b32_e32 v0, 0x2000
	global_load_dword v0, v0, s[2:3] offset:1024 sc1
	s_add_u32 s10, s2, 0x2400
	s_addc_u32 s11, s3, 0
	s_waitcnt vmcnt(0)
	v_cmp_eq_u32_e32 vcc, v0, v1
	s_and_saveexec_b64 s[6:7], vcc
	s_cbranch_execz .LBB0_3207
	s_mov_b32 s24, 1
	s_mov_b64 s[12:13], 0
	v_mov_b32_e32 v0, 0
	s_branch .LBB0_3198

.LBB0_3362:
	s_or_b64 exec, exec, s[8:9]
	v_cvt_f32_u32_e32 v4, v2
	s_waitcnt vmcnt(1)
	v_readfirstlane_b32 s4, v3
	v_sub_u32_e32 v3, 0, v2
	v_rcp_iflag_f32_e32 v4, v4
	v_add_u32_e32 v5, s4, v1
	v_mul_f32_e32 v4, 0x4f7ffffe, v4
	v_cvt_u32_f32_e32 v4, v4
	v_mul_lo_u32 v1, v3, v4
	v_mul_hi_u32 v1, v4, v1
	v_add_u32_e32 v1, v4, v1
	v_mul_hi_u32 v1, v5, v1
	v_mul_lo_u32 v3, v1, v2
	v_sub_u32_e32 v3, v5, v3
	v_add_u32_e32 v4, 1, v1
	v_cmp_ge_u32_e32 vcc, v3, v2
	s_nop 1
	v_cndmask_b32_e32 v1, v1, v4, vcc
	v_sub_u32_e32 v4, v3, v2
	v_cndmask_b32_e32 v3, v3, v4, vcc
	v_add_u32_e32 v4, 1, v1
	v_cmp_ge_u32_e32 vcc, v3, v2
	v_add_u32_e32 v3, 1, v5
	s_nop 0
	v_cndmask_b32_e32 v1, v1, v4, vcc
	v_mul_lo_u32 v4, v2, v1
	v_add_u32_e32 v2, v4, v2
	v_readfirstlane_b32 s99, v1
	v_cmp_ne_u32_e32 vcc, v3, v2
	s_and_saveexec_b64 s[4:5], vcc
	s_xor_b64 s[4:5], exec, s[4:5]
	s_cbranch_execz .LBB0_3376
	s_waitcnt lgkmcnt(0)
	v_mov_b32_e32 v0, 0x2000
	global_load_dword v0, v0, s[2:3] offset:1024 sc1
	s_add_u32 s10, s2, 0x2400
	s_addc_u32 s11, s3, 0
	s_waitcnt vmcnt(0)
	v_cmp_eq_u32_e32 vcc, v0, v1
	s_and_saveexec_b64 s[8:9], vcc
	s_cbranch_execz .LBB0_3375
	s_mov_b32 s26, 1
	s_mov_b64 s[12:13], 0
	v_mov_b32_e32 v0, 0
	s_branch .LBB0_3366

.LBB0_3452:
	s_or_b64 exec, exec, s[8:9]
	v_cvt_f32_u32_e32 v4, v2
	s_waitcnt vmcnt(1)
	v_readfirstlane_b32 s6, v3
	v_sub_u32_e32 v3, 0, v2
	v_rcp_iflag_f32_e32 v4, v4
	v_add_u32_e32 v5, s6, v1
	v_mul_f32_e32 v4, 0x4f7ffffe, v4
	v_cvt_u32_f32_e32 v4, v4
	v_mul_lo_u32 v1, v3, v4
	v_mul_hi_u32 v1, v4, v1
	v_add_u32_e32 v1, v4, v1
	v_mul_hi_u32 v1, v5, v1
	v_mul_lo_u32 v3, v1, v2
	v_sub_u32_e32 v3, v5, v3
	v_add_u32_e32 v4, 1, v1
	v_cmp_ge_u32_e32 vcc, v3, v2
	s_nop 1
	v_cndmask_b32_e32 v1, v1, v4, vcc
	v_sub_u32_e32 v4, v3, v2
	v_cndmask_b32_e32 v3, v3, v4, vcc
	v_add_u32_e32 v4, 1, v1
	v_cmp_ge_u32_e32 vcc, v3, v2
	v_add_u32_e32 v3, 1, v5
	s_nop 0
	v_cndmask_b32_e32 v1, v1, v4, vcc
	v_mul_lo_u32 v4, v2, v1
	v_add_u32_e32 v2, v4, v2
	v_readfirstlane_b32 s99, v1
	v_cmp_ne_u32_e32 vcc, v3, v2
	s_and_saveexec_b64 s[6:7], vcc
	s_xor_b64 s[6:7], exec, s[6:7]
	s_cbranch_execz .LBB0_3466
	s_waitcnt lgkmcnt(0)
	v_mov_b32_e32 v0, 0x2000
	global_load_dword v0, v0, s[4:5] offset:1024 sc1
	s_add_u32 s10, s4, 0x2400
	s_addc_u32 s11, s5, 0
	s_waitcnt vmcnt(0)
	v_cmp_eq_u32_e32 vcc, v0, v1
	s_and_saveexec_b64 s[8:9], vcc
	s_cbranch_execz .LBB0_3465
	s_mov_b32 s26, 1
	s_mov_b64 s[12:13], 0
	v_mov_b32_e32 v0, 0
	s_branch .LBB0_3456
